# speedup vs baseline: 1.0036x; 1.0036x over previous
.Lmy_ffn_noprio:
	s_lshl_b32 s6, s6, 13
	s_cmp_lg_u32 0, -1
	s_cselect_b32 s7, 0, 0
	s_add_i32 s10, s7, s6
	s_mov_b64 s[6:7], 0x2000
	s_add_i32 s8, s10, 0x13400
	v_lshl_add_u64 v[24:25], v[180:181], 0, s[6:7]
	s_mov_b32 s9, m0
	s_mov_b32 m0, s8
	s_nop 0
	global_load_lds_dwordx4 v[24:25], off
	s_mov_b32 m0, s9
	s_mov_b64 s[8:9], 0xa000
	v_lshl_add_u64 v[24:25], v[180:181], 0, s[8:9]
	s_add_i32 s8, s10, 0x13800
	s_mov_b32 s9, m0
	s_mov_b32 m0, s8
	s_nop 0
	global_load_lds_dwordx4 v[24:25], off
	s_mov_b32 m0, s9
	s_mov_b64 s[8:9], 0x2400
	s_add_i32 s11, s10, 0x13c00
	v_lshl_add_u64 v[24:25], v[180:181], 0, s[8:9]
	s_mov_b32 s8, m0
	s_mov_b32 m0, s11
	s_nop 0
	global_load_lds_dwordx4 v[24:25], off
	s_mov_b32 m0, s8
	s_mov_b64 s[8:9], 0xa400
	v_lshl_add_u64 v[24:25], v[180:181], 0, s[8:9]
	s_add_i32 s8, s10, 0x14000
	s_mov_b32 s9, m0
	s_mov_b32 m0, s8
	s_nop 0
	global_load_lds_dwordx4 v[24:25], off
	s_mov_b32 m0, s9
	s_mov_b64 s[8:9], 0x2800
	s_add_i32 s11, s10, 0x14400
	v_lshl_add_u64 v[24:25], v[180:181], 0, s[8:9]
	s_mov_b32 s8, m0
	s_mov_b32 m0, s11
	s_nop 0
	global_load_lds_dwordx4 v[24:25], off
	s_mov_b32 m0, s8
	s_mov_b64 s[8:9], 0xa800
	v_lshl_add_u64 v[24:25], v[180:181], 0, s[8:9]
	s_add_i32 s8, s10, 0x14800
	s_mov_b32 s9, m0
	s_mov_b32 m0, s8
	s_nop 0
	global_load_lds_dwordx4 v[24:25], off
	s_mov_b32 m0, s9
	s_mov_b64 s[8:9], 0x2c00
	s_add_i32 s11, s10, 0x14c00
	v_lshl_add_u64 v[24:25], v[180:181], 0, s[8:9]
	s_mov_b32 s8, m0
	s_mov_b32 m0, s11
	s_nop 0
	global_load_lds_dwordx4 v[24:25], off
	s_mov_b32 m0, s8
	s_mov_b64 s[8:9], 0xac00
	v_lshl_add_u64 v[24:25], v[180:181], 0, s[8:9]
	s_add_i32 s9, 0, 0x11400
	v_lshl_add_u32 v19, v37, 2, s9
	s_add_i32 s10, s10, 0x15000
	s_mov_b32 s8, m0
	s_mov_b32 m0, s10
	s_nop 0
	global_load_lds_dwordx4 v[24:25], off
	s_mov_b32 m0, s8
	s_waitcnt vmcnt(8)
	ds_write_b128 v19, v[20:23]
	v_lshrrev_b32_e32 v19, 5, v0
	v_mul_u32_u24_e32 v19, 0x410, v19
	v_and_b32_e32 v18, 0x1f0, v18
	v_add3_u32 v19, 0, v19, v18
	ds_write_b128 v19, v[14:17] offset:512
	v_lshrrev_b32_e32 v14, 5, v186
	v_mul_u32_u24_e32 v14, 0x410, v14
	v_add3_u32 v14, 0, v14, v18
	ds_write_b128 v14, v[6:9] offset:512
	v_lshrrev_b32_e32 v6, 5, v182
	v_mul_u32_u24_e32 v6, 0x410, v6
	v_add3_u32 v6, 0, v6, v18
	s_movk_i32 s10, 0x410
	ds_write_b128 v6, v[2:5] offset:512
	v_lshrrev_b32_e32 v2, 5, v185
	v_mul_u32_u24_e32 v2, 0x410, v2
	v_mad_u32_u24 v189, v205, s10, 0
	v_add3_u32 v2, 0, v2, v18
	v_lshl_add_u32 v202, v208, 4, v189
	ds_write_b128 v2, v[10:13] offset:512
	s_waitcnt lgkmcnt(0)
	s_barrier
	ds_read_b128 v[2:5], v202 offset:512
	ds_read_b128 v[102:105], v202 offset:544
	ds_read_b128 v[6:9], v202 offset:33792
	ds_read_b128 v[106:109], v202 offset:33824
	v_mul_u32_u24_e32 v187, 0x410, v205
	global_load_dwordx4 v[110:113], v[128:129], off
	s_waitcnt vmcnt(8) lgkmcnt(3)
	v_mfma_f32_32x32x16_f16 v[18:33], v[38:41], v[2:5], 0
	ds_read_b128 v[114:117], v202 offset:576
	ds_read_b128 v[118:121], v202 offset:33856
	s_waitcnt lgkmcnt(3)
	v_mfma_f32_32x32x16_f16 v[2:17], v[38:41], v[6:9], 0
	global_load_dwordx4 v[38:41], v[128:129], off offset:1024
	s_waitcnt vmcnt(8)
	v_mfma_f32_32x32x16_f16 v[18:33], v[42:45], v[102:105], v[18:33]
	ds_read_b128 v[102:105], v202 offset:608
	ds_read_b128 v[122:125], v202 offset:33888
	s_waitcnt lgkmcnt(4)
	v_mfma_f32_32x32x16_f16 v[2:17], v[42:45], v[106:109], v[2:17]
	global_load_dwordx4 v[42:45], v[128:129], off offset:2048
	s_waitcnt vmcnt(8) lgkmcnt(3)
	v_mfma_f32_32x32x16_f16 v[18:33], v[46:49], v[114:117], v[18:33]
	ds_read_b128 v[106:109], v202 offset:640
	ds_read_b128 v[114:117], v202 offset:33920
	s_waitcnt lgkmcnt(4)
	v_mfma_f32_32x32x16_f16 v[2:17], v[46:49], v[118:121], v[2:17]
	global_load_dwordx4 v[46:49], v[128:129], off offset:3072
	s_waitcnt vmcnt(8) lgkmcnt(3)
	v_mfma_f32_32x32x16_f16 v[18:33], v[50:53], v[102:105], v[18:33]
	ds_read_b128 v[102:105], v202 offset:672
	ds_read_b128 v[118:121], v202 offset:33952
	s_waitcnt lgkmcnt(4)
	v_mfma_f32_32x32x16_f16 v[2:17], v[50:53], v[122:125], v[2:17]
	s_movk_i32 s8, 0x3000
	v_add_co_u32_e32 v126, vcc, s8, v126
	s_waitcnt vmcnt(7) lgkmcnt(3)
	v_mfma_f32_32x32x16_f16 v[18:33], v[54:57], v[106:109], v[18:33]
	v_addc_co_u32_e32 v127, vcc, 0, v127, vcc
	global_load_dwordx4 v[50:53], v[126:127], off
	ds_read_b128 v[106:109], v202 offset:704
	ds_read_b128 v[122:125], v202 offset:33984
	s_waitcnt lgkmcnt(4)
	v_mfma_f32_32x32x16_f16 v[2:17], v[54:57], v[114:117], v[2:17]
	global_load_dwordx4 v[54:57], v[126:127], off offset:1024
	s_waitcnt vmcnt(8) lgkmcnt(3)
	v_mfma_f32_32x32x16_f16 v[18:33], v[58:61], v[102:105], v[18:33]
	ds_read_b128 v[102:105], v202 offset:736
	ds_read_b128 v[114:117], v202 offset:34016
	s_waitcnt lgkmcnt(4)
	v_mfma_f32_32x32x16_f16 v[2:17], v[58:61], v[118:121], v[2:17]
	global_load_dwordx4 v[58:61], v[126:127], off offset:2048
	s_waitcnt vmcnt(8) lgkmcnt(3)
	v_mfma_f32_32x32x16_f16 v[18:33], v[62:65], v[106:109], v[18:33]
	ds_read_b128 v[106:109], v202 offset:768
	ds_read_b128 v[118:121], v202 offset:34048
	s_waitcnt lgkmcnt(4)
	v_mfma_f32_32x32x16_f16 v[2:17], v[62:65], v[122:125], v[2:17]
	global_load_dwordx4 v[62:65], v[126:127], off offset:3072
	s_waitcnt vmcnt(8) lgkmcnt(3)
	v_mfma_f32_32x32x16_f16 v[18:33], v[98:101], v[102:105], v[18:33]
	ds_read_b128 v[102:105], v202 offset:800
	ds_read_b128 v[122:125], v202 offset:34080
	s_waitcnt lgkmcnt(4)
	v_mfma_f32_32x32x16_f16 v[2:17], v[98:101], v[114:117], v[2:17]
	s_waitcnt vmcnt(7) lgkmcnt(3)
	v_mfma_f32_32x32x16_f16 v[18:33], v[110:113], v[106:109], v[18:33]
	ds_read_b128 v[98:101], v202 offset:832
	ds_read_b128 v[106:109], v202 offset:34112
	s_waitcnt lgkmcnt(4)
	v_mfma_f32_32x32x16_f16 v[2:17], v[110:113], v[118:121], v[2:17]
	s_waitcnt vmcnt(6) lgkmcnt(3)
	v_mfma_f32_32x32x16_f16 v[18:33], v[38:41], v[102:105], v[18:33]
	ds_read_b128 v[102:105], v202 offset:864
	ds_read_b128 v[110:113], v202 offset:34144
	s_waitcnt lgkmcnt(4)
	v_mfma_f32_32x32x16_f16 v[2:17], v[38:41], v[122:125], v[2:17]
	s_waitcnt vmcnt(5) lgkmcnt(3)
	v_mfma_f32_32x32x16_f16 v[18:33], v[42:45], v[98:101], v[18:33]
	ds_read_b128 v[38:41], v202 offset:896
	ds_read_b128 v[98:101], v202 offset:34176
	s_waitcnt lgkmcnt(4)
	v_mfma_f32_32x32x16_f16 v[2:17], v[42:45], v[106:109], v[2:17]
	s_waitcnt vmcnt(4) lgkmcnt(3)
	v_mfma_f32_32x32x16_f16 v[18:33], v[46:49], v[102:105], v[18:33]
	ds_read_b128 v[42:45], v202 offset:928
	ds_read_b128 v[102:105], v202 offset:34208
	s_waitcnt lgkmcnt(4)
	v_mfma_f32_32x32x16_f16 v[2:17], v[46:49], v[110:113], v[2:17]
	s_waitcnt vmcnt(3) lgkmcnt(3)
	v_mfma_f32_32x32x16_f16 v[18:33], v[50:53], v[38:41], v[18:33]
	ds_read_b128 v[38:41], v202 offset:960
	ds_read_b128 v[46:49], v202 offset:34240
	s_waitcnt lgkmcnt(4)
	v_mfma_f32_32x32x16_f16 v[2:17], v[50:53], v[98:101], v[2:17]
	s_waitcnt vmcnt(2) lgkmcnt(3)
	v_mfma_f32_32x32x16_f16 v[18:33], v[54:57], v[42:45], v[18:33]
	ds_read_b128 v[42:45], v202 offset:992
	ds_read_b128 v[50:53], v202 offset:34272
	s_waitcnt lgkmcnt(4)
	v_mfma_f32_32x32x16_f16 v[2:17], v[54:57], v[102:105], v[2:17]
	s_waitcnt vmcnt(1) lgkmcnt(3)
	v_mfma_f32_32x32x16_f16 v[18:33], v[58:61], v[38:41], v[18:33]
	s_waitcnt lgkmcnt(2)
	v_mfma_f32_32x32x16_f16 v[2:17], v[58:61], v[46:49], v[2:17]
	s_waitcnt vmcnt(0) lgkmcnt(1)
	v_mfma_f32_32x32x16_f16 v[18:33], v[62:65], v[42:45], v[18:33]
	s_waitcnt lgkmcnt(0)
	v_mfma_f32_32x32x16_f16 v[2:17], v[62:65], v[50:53], v[2:17]
	s_mov_b64 s[20:21], 0x8000
	v_lshl_add_u64 v[114:115], v[180:181], 0, s[20:21]
	s_mov_b64 s[22:23], 0x1000
	v_lshl_add_u64 v[116:117], v[180:181], 0, s[22:23]
	v_lshl_add_u64 v[118:119], v[114:115], 0, s[22:23]
	global_load_dwordx4 v[214:217], v[180:181], off
	global_load_dwordx4 v[102:105], v[114:115], off
	global_load_dwordx4 v[106:109], v[180:181], off offset:1024
	global_load_dwordx4 v[110:113], v[114:115], off offset:1024
	global_load_dwordx4 v[122:125], v[180:181], off offset:2048
	global_load_dwordx4 v[126:129], v[114:115], off offset:2048
	global_load_dwordx4 v[130:133], v[180:181], off offset:3072
	global_load_dwordx4 v[134:137], v[114:115], off offset:3072
	global_load_dwordx4 v[138:141], v[116:117], off
	global_load_dwordx4 v[142:145], v[118:119], off
	global_load_dwordx4 v[150:153], v[116:117], off offset:1024
	global_load_dwordx4 v[154:157], v[118:119], off offset:1024
	global_load_dwordx4 v[158:161], v[116:117], off offset:2048
	global_load_dwordx4 v[162:165], v[118:119], off offset:2048
	global_load_dwordx4 v[166:169], v[116:117], off offset:3072
	global_load_dwordx4 v[210:213], v[118:119], off offset:3072
	v_and_b32_e32 v188, 0xfc, v37
	v_lshl_add_u32 v35, v188, 1, 0
	v_cvt_pk_f16_f32 v39, v92, v93
	v_cvt_pk_f16_f32 v38, v90, v91
	v_mad_u32_u24 v37, v209, s10, v35
	ds_write_b64 v37, v[38:39]
	v_lshrrev_b32_e32 v37, 6, v186
	v_cvt_pk_f16_f32 v39, v96, v97
	v_cvt_pk_f16_f32 v38, v94, v95
	v_mad_u32_u24 v40, v37, s10, v35
	v_lshrrev_b32_e32 v44, 6, v182
	ds_write_b64 v40, v[38:39]
	v_cvt_pk_f16_f32 v39, v88, v89
	v_cvt_pk_f16_f32 v38, v86, v87
	v_mad_u32_u24 v40, v44, s10, v35
	v_lshrrev_b32_e32 v45, 6, v185
	ds_write_b64 v40, v[38:39]
	v_cvt_pk_f16_f32 v39, v84, v85
	v_cvt_pk_f16_f32 v38, v82, v83
	v_mad_u32_u24 v40, v45, s10, v35
	v_lshrrev_b32_e32 v46, 6, v179
	ds_write_b64 v40, v[38:39]
	v_cvt_pk_f16_f32 v39, v80, v81
	v_cvt_pk_f16_f32 v38, v78, v79
	v_mad_u32_u24 v40, v46, s10, v35
	v_lshrrev_b32_e32 v47, 6, v184
	ds_write_b64 v40, v[38:39]
	v_cvt_pk_f16_f32 v39, v76, v77
	v_cvt_pk_f16_f32 v38, v74, v75
	v_mad_u32_u24 v40, v47, s10, v35
	v_lshrrev_b32_e32 v48, 6, v1
	ds_write_b64 v40, v[38:39]
	v_cvt_pk_f16_f32 v39, v72, v73
	v_cvt_pk_f16_f32 v38, v70, v71
	v_mad_u32_u24 v40, v48, s10, v35
	v_lshrrev_b32_e32 v49, 6, v183
	v_lshlrev_b32_e32 v207, 2, v208
	ds_write_b64 v40, v[38:39]
	v_cvt_pk_f16_f32 v39, v68, v69
	v_cvt_pk_f16_f32 v38, v66, v67
	v_mad_u32_u24 v35, v49, s10, v35
	v_lshl_or_b32 v191, v209, 5, v207
	ds_write_b64 v35, v[38:39]
	v_lshl_add_u32 v35, v191, 2, s9
	v_or_b32_e32 v194, 8, v191
	v_or_b32_e32 v200, 16, v191
	v_or_b32_e32 v201, 24, v191
	ds_read_b128 v[50:53], v35
	v_lshl_add_u32 v35, v194, 2, s9
	ds_read_b128 v[54:57], v35
	v_lshl_add_u32 v35, v200, 2, s9
	ds_read_b128 v[58:61], v35
	v_lshl_add_u32 v35, v201, 2, s9
	ds_read_b128 v[62:65], v35
	v_lshl_add_u32 v35, v191, 1, v189
	s_waitcnt lgkmcnt(0)
	s_barrier
	v_add_f32_e32 v18, v50, v18
	v_add_f32_e32 v19, v51, v19
	v_add_f32_e32 v20, v52, v20
	v_add_f32_e32 v21, v53, v21
	v_cvt_pk_f16_f32 v18, v18, v19
	v_cvt_pk_f16_f32 v19, v20, v21
	ds_write_b64 v35, v[18:19] offset:512
	v_add_f32_e32 v2, v50, v2
	v_add_f32_e32 v3, v51, v3
	v_add_f32_e32 v4, v52, v4
	v_add_f32_e32 v5, v53, v5
	v_cvt_pk_f16_f32 v2, v2, v3
	v_cvt_pk_f16_f32 v3, v4, v5
	ds_write_b64 v35, v[2:3] offset:33792
	v_add_f32_e32 v22, v54, v22
	v_add_f32_e32 v23, v55, v23
	v_add_f32_e32 v24, v56, v24
	v_add_f32_e32 v25, v57, v25
	v_cvt_pk_f16_f32 v22, v22, v23
	v_cvt_pk_f16_f32 v23, v24, v25
	ds_write_b64 v35, v[22:23] offset:528
	v_add_f32_e32 v6, v54, v6
	v_add_f32_e32 v7, v55, v7
	v_add_f32_e32 v8, v56, v8
	v_add_f32_e32 v9, v57, v9
	v_cvt_pk_f16_f32 v6, v6, v7
	v_cvt_pk_f16_f32 v7, v8, v9
	ds_write_b64 v35, v[6:7] offset:33808
	v_add_f32_e32 v26, v58, v26
	v_add_f32_e32 v27, v59, v27
	v_add_f32_e32 v28, v60, v28
	v_add_f32_e32 v29, v61, v29
	v_cvt_pk_f16_f32 v26, v26, v27
	v_cvt_pk_f16_f32 v27, v28, v29
	ds_write_b64 v35, v[26:27] offset:544
	v_add_f32_e32 v10, v58, v10
	v_add_f32_e32 v11, v59, v11
	v_add_f32_e32 v12, v60, v12
	v_add_f32_e32 v13, v61, v13
	v_cvt_pk_f16_f32 v10, v10, v11
	v_cvt_pk_f16_f32 v11, v12, v13
	ds_write_b64 v35, v[10:11] offset:33824
	v_add_f32_e32 v30, v62, v30
	v_add_f32_e32 v31, v63, v31
	v_add_f32_e32 v32, v64, v32
	v_add_f32_e32 v33, v65, v33
	v_cvt_pk_f16_f32 v30, v30, v31
	v_cvt_pk_f16_f32 v31, v32, v33
	ds_write_b64 v35, v[30:31] offset:560
	v_add_f32_e32 v14, v62, v14
	v_add_f32_e32 v15, v63, v15
	v_add_f32_e32 v16, v64, v16
	v_add_f32_e32 v17, v65, v17
	v_cvt_pk_f16_f32 v14, v14, v15
	v_cvt_pk_f16_f32 v15, v16, v17
	ds_write_b64 v35, v[14:15] offset:33840
	s_mov_b32 s15, 0x9000
	v_mul_u32_u24_e32 v199, 0x410, v209
	v_mul_u32_u24_e32 v198, 0x410, v37
	v_mul_u32_u24_e32 v197, 0x410, v44
	v_mul_u32_u24_e32 v195, 0x410, v45
	v_mul_u32_u24_e32 v196, 0x410, v46
	v_mul_u32_u24_e32 v193, 0x410, v47
	v_mul_u32_u24_e32 v192, 0x410, v48
	v_mul_u32_u24_e32 v190, 0x410, v49
	s_mov_b32 s9, 0x8000
	s_waitcnt lgkmcnt(0)
	s_barrier
	ds_read_b128 v[2:5], v202
	ds_read_b128 v[114:117], v202 offset:32
	ds_read_b128 v[6:9], v202 offset:33280
	ds_read_b128 v[146:149], v202 offset:33312
	s_add_i32 s9, 0, 0x13400
	v_add3_u32 v204, s9, v36, v34
	s_waitcnt vmcnt(15) lgkmcnt(3)
	v_mfma_f32_32x32x16_f16 v[50:65], v[214:217], v[2:5], 0
	ds_read_b128 v[170:173], v202 offset:64
	ds_read_b128 v[174:177], v202 offset:33344
	ds_read_b128 v[118:121], v204
	ds_read_b128 v[98:101], v204 offset:1024
	s_waitcnt lgkmcnt(5)
	v_mfma_f32_32x32x16_f16 v[34:49], v[214:217], v[6:9], 0
	s_waitcnt vmcnt(14)
	v_mfma_f32_32x32x16_f16 v[18:33], v[102:105], v[2:5], 0
	v_mfma_f32_32x32x16_f16 v[2:17], v[102:105], v[6:9], 0
	s_waitcnt vmcnt(13)
	v_mfma_f32_32x32x16_f16 v[50:65], v[106:109], v[114:117], v[50:65]
	s_waitcnt lgkmcnt(4)
	v_mfma_f32_32x32x16_f16 v[34:49], v[106:109], v[146:149], v[34:49]
	s_waitcnt vmcnt(12)
	v_mfma_f32_32x32x16_f16 v[18:33], v[110:113], v[114:117], v[18:33]
	ds_read_b128 v[214:217], v202 offset:96
	ds_read_b128 v[218:221], v202 offset:33376
	ds_read_b128 v[114:117], v204 offset:2048
	ds_read_b128 v[102:105], v204 offset:3072
	v_mfma_f32_32x32x16_f16 v[2:17], v[110:113], v[146:149], v[2:17]
	s_waitcnt vmcnt(11) lgkmcnt(7)
	v_mfma_f32_32x32x16_f16 v[50:65], v[122:125], v[170:173], v[50:65]
	s_waitcnt lgkmcnt(6)
	v_mfma_f32_32x32x16_f16 v[34:49], v[122:125], v[174:177], v[34:49]
	s_waitcnt vmcnt(10)
	v_mfma_f32_32x32x16_f16 v[18:33], v[126:129], v[170:173], v[18:33]
	ds_read_b128 v[146:149], v202 offset:128
	ds_read_b128 v[170:173], v202 offset:33408
	ds_read_b128 v[122:125], v204 offset:4096
	ds_read_b128 v[106:109], v204 offset:5120
	v_mfma_f32_32x32x16_f16 v[2:17], v[126:129], v[174:177], v[2:17]
	s_waitcnt vmcnt(9) lgkmcnt(7)
	v_mfma_f32_32x32x16_f16 v[50:65], v[130:133], v[214:217], v[50:65]
	s_waitcnt lgkmcnt(6)
	v_mfma_f32_32x32x16_f16 v[34:49], v[130:133], v[218:221], v[34:49]
	ds_read_b128 v[130:133], v202 offset:160
	ds_read_b128 v[174:177], v202 offset:33440
	ds_read_b128 v[126:129], v204 offset:6144
	ds_read_b128 v[110:113], v204 offset:7168
	s_waitcnt vmcnt(8)
	v_mfma_f32_32x32x16_f16 v[18:33], v[134:137], v[214:217], v[18:33]
	v_mfma_f32_32x32x16_f16 v[2:17], v[134:137], v[218:221], v[2:17]
	v_add_co_u32_e32 v226, vcc, s8, v180
	s_mov_b32 s8, 0xb000
	s_nop 0
	v_addc_co_u32_e32 v227, vcc, 0, v181, vcc
	v_add_co_u32_e32 v228, vcc, s8, v180
	s_waitcnt vmcnt(7) lgkmcnt(7)
	v_mfma_f32_32x32x16_f16 v[50:65], v[138:141], v[146:149], v[50:65]
	v_addc_co_u32_e32 v229, vcc, 0, v181, vcc
	s_waitcnt vmcnt(6)
	v_mfma_f32_32x32x16_f16 v[18:33], v[142:145], v[146:149], v[18:33]
	global_load_dwordx4 v[146:149], v[226:227], off
	global_load_dwordx4 v[134:137], v[228:229], off
	s_waitcnt lgkmcnt(6)
	v_mfma_f32_32x32x16_f16 v[34:49], v[138:141], v[170:173], v[34:49]
	ds_read_b128 v[138:141], v202 offset:192
	ds_read_b128 v[214:217], v202 offset:33472
	v_mfma_f32_32x32x16_f16 v[2:17], v[142:145], v[170:173], v[2:17]
	s_waitcnt vmcnt(7) lgkmcnt(5)
	v_mfma_f32_32x32x16_f16 v[50:65], v[150:153], v[130:133], v[50:65]
	s_waitcnt vmcnt(6)
	v_mfma_f32_32x32x16_f16 v[18:33], v[154:157], v[130:133], v[18:33]
	global_load_dwordx4 v[142:145], v[226:227], off offset:1024
	global_load_dwordx4 v[130:133], v[228:229], off offset:1024
	ds_read_b128 v[218:221], v202 offset:224
	ds_read_b128 v[222:225], v202 offset:33504
	s_waitcnt lgkmcnt(6)
	v_mfma_f32_32x32x16_f16 v[34:49], v[150:153], v[174:177], v[34:49]
	v_mfma_f32_32x32x16_f16 v[2:17], v[154:157], v[174:177], v[2:17]
	s_waitcnt vmcnt(7) lgkmcnt(3)
	v_mfma_f32_32x32x16_f16 v[50:65], v[158:161], v[138:141], v[50:65]
	s_waitcnt vmcnt(6)
	v_mfma_f32_32x32x16_f16 v[18:33], v[162:165], v[138:141], v[18:33]
	global_load_dwordx4 v[150:153], v[226:227], off offset:2048
	global_load_dwordx4 v[138:141], v[228:229], off offset:2048
	ds_read_b128 v[174:177], v202 offset:256
	ds_read_b128 v[170:173], v202 offset:33536
	s_waitcnt lgkmcnt(4)
	v_mfma_f32_32x32x16_f16 v[34:49], v[158:161], v[214:217], v[34:49]
	v_mfma_f32_32x32x16_f16 v[2:17], v[162:165], v[214:217], v[2:17]
	global_load_dwordx4 v[158:161], v[226:227], off offset:3072
	global_load_dwordx4 v[154:157], v[228:229], off offset:3072
	s_waitcnt vmcnt(9) lgkmcnt(3)
	v_mfma_f32_32x32x16_f16 v[50:65], v[166:169], v[218:221], v[50:65]
	s_waitcnt lgkmcnt(2)
	v_mfma_f32_32x32x16_f16 v[34:49], v[166:169], v[222:225], v[34:49]
	ds_read_b128 v[166:169], v202 offset:288
	ds_read_b128 v[162:165], v202 offset:33568
	s_waitcnt vmcnt(8)
	v_mfma_f32_32x32x16_f16 v[18:33], v[210:213], v[218:221], v[18:33]
	v_mfma_f32_32x32x16_f16 v[2:17], v[210:213], v[222:225], v[2:17]
	s_mov_b64 s[8:9], 0x4000
	v_add_u32_e32 v203, 0x140, v202
	v_lshl_add_u64 v[180:181], v[180:181], 0, s[8:9]
	s_mov_b64 s[8:9], 0x8000
	s_mov_b64 s[10:11], 0x1000
	s_mov_b64 s[12:13], 0x9000
	v_mov_b32_e32 v210, v203

	.amdhsa_kernel _Z10ffn_kernelPKfS0_PKDF16_S2_S0_S2_S0_S0_S0_S2_S0_Pf
		.amdhsa_group_segment_fixed_size 0
		.amdhsa_private_segment_fixed_size 0
		.amdhsa_kernarg_size 96
		.amdhsa_user_sgpr_count 2
		.amdhsa_user_sgpr_dispatch_ptr 0
		.amdhsa_user_sgpr_queue_ptr 0
		.amdhsa_user_sgpr_kernarg_segment_ptr 1
		.amdhsa_user_sgpr_dispatch_id 0
		.amdhsa_user_sgpr_kernarg_preload_length 0
		.amdhsa_user_sgpr_kernarg_preload_offset 0
		.amdhsa_user_sgpr_private_segment_size 0
		.amdhsa_uses_dynamic_stack 0
		.amdhsa_enable_private_segment 0
		.amdhsa_system_sgpr_workgroup_id_x 1
		.amdhsa_system_sgpr_workgroup_id_y 0
		.amdhsa_system_sgpr_workgroup_id_z 0
		.amdhsa_system_sgpr_workgroup_info 0
		.amdhsa_system_vgpr_workitem_id 0
		.amdhsa_next_free_vgpr 230
		.amdhsa_next_free_sgpr 24
		.amdhsa_accum_offset 232
		.amdhsa_reserve_vcc 1
		.amdhsa_float_round_mode_32 0
		.amdhsa_float_round_mode_16_64 0
		.amdhsa_float_denorm_mode_32 3
		.amdhsa_float_denorm_mode_16_64 3
		.amdhsa_dx10_clamp 1
		.amdhsa_ieee_mode 1
		.amdhsa_fp16_overflow 0
		.amdhsa_tg_split 0
		.amdhsa_exception_fp_ieee_invalid_op 0
		.amdhsa_exception_fp_denorm_src 0
		.amdhsa_exception_fp_ieee_div_zero 0
		.amdhsa_exception_fp_ieee_overflow 0
		.amdhsa_exception_fp_ieee_underflow 0
		.amdhsa_exception_fp_ieee_inexact 0
		.amdhsa_exception_int_div_zero 0
	.end_amdhsa_kernel

amdhsa.kernels:
  - .agpr_count:     0
    .args:
      - .actual_access:  read_only
        .address_space:  global
        .offset:         0
        .size:           8
        .value_kind:     global_buffer
      - .actual_access:  read_only
        .address_space:  global
        .offset:         8
        .size:           8
        .value_kind:     global_buffer
      - .actual_access:  read_only
        .address_space:  global
        .offset:         16
        .size:           8
        .value_kind:     global_buffer
      - .actual_access:  read_only
        .address_space:  global
        .offset:         24
        .size:           8
        .value_kind:     global_buffer
      - .actual_access:  read_only
        .address_space:  global
        .offset:         32
        .size:           8
        .value_kind:     global_buffer
      - .actual_access:  write_only
        .address_space:  global
        .offset:         40
        .size:           8
        .value_kind:     global_buffer
      - .actual_access:  write_only
        .address_space:  global
        .offset:         48
        .size:           8
        .value_kind:     global_buffer
      - .actual_access:  write_only
        .address_space:  global
        .offset:         56
        .size:           8
        .value_kind:     global_buffer
      - .actual_access:  write_only
        .address_space:  global
        .offset:         64
        .size:           8
        .value_kind:     global_buffer
    .group_segment_fixed_size: 0
    .kernarg_segment_align: 8
    .kernarg_segment_size: 72
    .language:       OpenCL C
    .language_version:
      - 2
      - 0
    .max_flat_workgroup_size: 256
    .name:           _Z11prep_kernelPKfS0_S0_S0_S0_PDF16_S1_S1_S1_
    .private_segment_fixed_size: 0
    .sgpr_count:     21
    .sgpr_spill_count: 0
    .symbol:         _Z11prep_kernelPKfS0_S0_S0_S0_PDF16_S1_S1_S1_.kd
    .uniform_work_group_size: 1
    .uses_dynamic_stack: false
    .vgpr_count:     18
    .vgpr_spill_count: 0
    .wavefront_size: 64
  - .agpr_count:     0
    .args:
      - .actual_access:  read_only
        .address_space:  global
        .offset:         0
        .size:           8
        .value_kind:     global_buffer
      - .actual_access:  read_only
        .address_space:  global
        .offset:         8
        .size:           8
        .value_kind:     global_buffer
      - .actual_access:  read_only
        .address_space:  global
        .offset:         16
        .size:           8
        .value_kind:     global_buffer
      - .actual_access:  read_only
        .address_space:  global
        .offset:         24
        .size:           8
        .value_kind:     global_buffer
      - .actual_access:  read_only
        .address_space:  global
        .offset:         32
        .size:           8
        .value_kind:     global_buffer
      - .actual_access:  write_only
        .address_space:  global
        .offset:         40
        .size:           8
        .value_kind:     global_buffer
      - .actual_access:  write_only
        .address_space:  global
        .offset:         48
        .size:           8
        .value_kind:     global_buffer
    .group_segment_fixed_size: 0
    .kernarg_segment_align: 8
    .kernarg_segment_size: 56
    .language:       OpenCL C
    .language_version:
      - 2
      - 0
    .max_flat_workgroup_size: 512
    .name:           _Z11proj_kernelPKfS0_PKDF16_S0_S0_PDF16_S3_
    .private_segment_fixed_size: 0
    .sgpr_count:     22
    .sgpr_spill_count: 0
    .symbol:         _Z11proj_kernelPKfS0_PKDF16_S0_S0_PDF16_S3_.kd
    .uniform_work_group_size: 1
    .uses_dynamic_stack: false
    .vgpr_count:     170
    .vgpr_spill_count: 0
    .wavefront_size: 64
  - .agpr_count:     0
    .args:
      - .address_space:  global
        .offset:         0
        .size:           8
        .value_kind:     global_buffer
      - .address_space:  global
        .offset:         8
        .size:           8
        .value_kind:     global_buffer
      - .actual_access:  write_only
        .address_space:  global
        .offset:         16
        .size:           8
        .value_kind:     global_buffer
    .group_segment_fixed_size: 0
    .kernarg_segment_align: 8
    .kernarg_segment_size: 24
    .language:       OpenCL C
    .language_version:
      - 2
      - 0
    .max_flat_workgroup_size: 512
    .name:           _Z11attn_kernelPKDF16_S0_PDF16_
    .private_segment_fixed_size: 0
    .sgpr_count:     56
    .sgpr_spill_count: 0
    .symbol:         _Z11attn_kernelPKDF16_S0_PDF16_.kd
    .uniform_work_group_size: 1
    .uses_dynamic_stack: false
    .vgpr_count:     192
    .vgpr_spill_count: 0
    .wavefront_size: 64
  - .agpr_count:     0
    .args:
      - .actual_access:  read_only
        .address_space:  global
        .offset:         0
        .size:           8
        .value_kind:     global_buffer
      - .actual_access:  read_only
        .address_space:  global
        .offset:         8
        .size:           8
        .value_kind:     global_buffer
      - .actual_access:  read_only
        .address_space:  global
        .offset:         16
        .size:           8
        .value_kind:     global_buffer
      - .actual_access:  read_only
        .address_space:  global
        .offset:         24
        .size:           8
        .value_kind:     global_buffer
      - .actual_access:  read_only
        .address_space:  global
        .offset:         32
        .size:           8
        .value_kind:     global_buffer
      - .address_space:  global
        .offset:         40
        .size:           8
        .value_kind:     global_buffer
      - .actual_access:  read_only
        .address_space:  global
        .offset:         48
        .size:           8
        .value_kind:     global_buffer
      - .actual_access:  read_only
        .address_space:  global
        .offset:         56
        .size:           8
        .value_kind:     global_buffer
      - .actual_access:  read_only
        .address_space:  global
        .offset:         64
        .size:           8
        .value_kind:     global_buffer
      - .address_space:  global
        .offset:         72
        .size:           8
        .value_kind:     global_buffer
      - .actual_access:  read_only
        .address_space:  global
        .offset:         80
        .size:           8
        .value_kind:     global_buffer
      - .actual_access:  write_only
        .address_space:  global
        .offset:         88
        .size:           8
        .value_kind:     global_buffer
    .group_segment_fixed_size: 0
    .kernarg_segment_align: 8
    .kernarg_segment_size: 96
    .language:       OpenCL C
    .language_version:
      - 2
      - 0
    .max_flat_workgroup_size: 512
    .name:           _Z10ffn_kernelPKfS0_PKDF16_S2_S0_S2_S0_S0_S0_S2_S0_Pf
    .private_segment_fixed_size: 0
    .sgpr_count:     30
    .sgpr_spill_count: 0
    .symbol:         _Z10ffn_kernelPKfS0_PKDF16_S2_S0_S2_S0_S0_S0_S2_S0_Pf.kd
    .uniform_work_group_size: 1
    .uses_dynamic_stack: false
    .vgpr_count:     230
    .vgpr_spill_count: 0
    .wavefront_size: 64
